# wo: K-slab order rotated per XCD (4*(blockIdx&7)) to spread memory channels
# baseline (speedup 1.0000x reference)
.LBB2_2:
	s_and_b32 s11, s2, 7
	s_lshl_b32 s11, s11, 2
	s_lshl_b32 s12, s11, 7
	s_mov_b32 s13, 0
	s_add_i32 s14, s11, 1
	s_and_b32 s14, s14, 31
	s_lshl_b32 s14, s14, 7
	s_mov_b32 s15, 0
	s_add_i32 s16, s11, 2
	s_and_b32 s16, s16, 31
	s_lshl_b32 s16, s16, 7
	s_mov_b32 s17, 0
	s_lshl_b32 s0, s2, 2
	s_and_b32 s0, s0, 12
	s_bfe_u32 s1, s2, 0x20003
	s_or_b32 s0, s0, s1
	s_lshl_b32 s3, s0, 7
	s_lshl_b32 s0, s2, 1
	s_and_b32 s0, s0, 8
	s_lshr_b32 s1, s2, 5
	s_add_i32 s0, s0, s1
	s_lshl_b32 s2, s0, 7
	v_lshrrev_b32_e32 v32, 3, v0
	v_or_b32_e32 v2, s2, v32
	v_ashrrev_i32_e32 v3, 31, v2
	v_lshlrev_b64 v[2:3], 12, v[2:3]
	s_waitcnt lgkmcnt(0)
	v_lshl_add_u64 v[4:5], s[6:7], 0, v[2:3]
	v_lshlrev_b32_e32 v2, 4, v0
	v_or_b32_e32 v1, s3, v32
	v_and_b32_e32 v2, 0x70, v2
	v_mov_b32_e32 v3, 0
	v_lshl_add_u64 v[98:99], v[4:5], 0, v[2:3]
	v_lshlrev_b32_e32 v4, 12, v1
	v_mov_b32_e32 v5, v3
	v_lshl_add_u64 v[4:5], s[4:5], 0, v[4:5]
	v_lshl_add_u64 v[100:101], v[4:5], 0, v[2:3]
	s_mov_b32 s4, 0x40000
	v_add_co_u32_e32 v28, vcc, s4, v100
	v_lshl_add_u64 v[134:135], v[100:101], 0, s[12:13]
	global_load_dwordx4 v[12:15], v[134:135], off
	v_lshl_add_u64 v[134:135], v[98:99], 0, s[12:13]
	global_load_dwordx4 v[16:19], v[134:135], off
	v_addc_co_u32_e32 v29, vcc, 0, v101, vcc
	v_add_co_u32_e32 v30, vcc, s4, v98
	v_lshl_add_u64 v[134:135], v[28:29], 0, s[12:13]
	global_load_dwordx4 v[20:23], v[134:135], off
	s_nop 0
	v_addc_co_u32_e32 v31, vcc, 0, v99, vcc
	v_lshl_add_u64 v[134:135], v[30:31], 0, s[12:13]
	global_load_dwordx4 v[24:27], v[134:135], off
	v_lshl_add_u64 v[134:135], v[100:101], 0, s[14:15]
	global_load_dwordx4 v[66:69], v[134:135], off
	v_lshl_add_u64 v[134:135], v[98:99], 0, s[14:15]
	global_load_dwordx4 v[70:73], v[134:135], off
	v_lshl_add_u64 v[134:135], v[100:101], 0, s[16:17]
	global_load_dwordx4 v[74:77], v[134:135], off
	v_lshl_add_u64 v[134:135], v[28:29], 0, s[14:15]
	global_load_dwordx4 v[82:85], v[134:135], off
	v_lshl_add_u64 v[134:135], v[28:29], 0, s[16:17]
	global_load_dwordx4 v[86:89], v[134:135], off
	v_lshl_add_u64 v[134:135], v[98:99], 0, s[16:17]
	global_load_dwordx4 v[78:81], v[134:135], off
	v_lshl_add_u64 v[134:135], v[30:31], 0, s[14:15]
	global_load_dwordx4 v[90:93], v[134:135], off
	v_lshl_add_u64 v[134:135], v[30:31], 0, s[16:17]
	global_load_dwordx4 v[94:97], v[134:135], off
	v_lshrrev_b32_e32 v2, 4, v0
	v_lshrrev_b32_e32 v104, 6, v0
	v_lshrrev_b32_e32 v105, 8, v0
	v_xor_b32_e32 v2, v2, v0
	v_bfe_u32 v103, v0, 5, 1
	v_lshlrev_b32_e32 v34, 2, v105
	v_lshlrev_b32_e32 v102, 5, v104
	v_lshlrev_b32_e32 v2, 4, v2
	v_and_b32_e32 v1, 31, v0
	v_bfe_u32 v33, v0, 1, 3
	v_lshlrev_b32_e32 v4, 7, v0
	v_or_b32_e32 v36, v34, v103
	v_and_b32_e32 v106, 64, v102
	v_and_b32_e32 v2, 0x70, v2
	v_and_b32_e32 v35, 0x2f80, v4
	v_bitop3_b32 v28, v34, v33, v103 bitop3:0x36
	v_bitop3_b32 v30, v36, v33, 2 bitop3:0x36
	v_or_b32_e32 v31, v106, v1
	v_lshl_or_b32 v2, v32, 7, v2
	v_add_u32_e32 v29, 0, v35
	v_lshlrev_b32_e32 v28, 4, v28
	v_lshl_add_u32 v31, v31, 7, 0
	v_lshlrev_b32_e32 v30, 4, v30
	v_add_u32_e32 v108, 0, v2
	s_mov_b32 s1, 0
	s_mov_b32 s5, -2
	v_mov_b32_e32 v4, v3
	v_mov_b32_e32 v5, v3
	v_mov_b32_e32 v6, v3
	v_mov_b32_e32 v7, v3
	v_mov_b32_e32 v8, v3
	v_mov_b32_e32 v9, v3
	v_mov_b32_e32 v10, v3
	v_mov_b32_e32 v11, v3
	v_add_u32_e32 v107, v29, v28
	v_add_u32_e32 v109, v31, v28
	v_add_u32_e32 v110, v31, v30
	v_add_u32_e32 v111, v29, v30
	v_mov_b32_e32 v2, v3
	v_mov_b32_e32 v28, v3
	v_mov_b32_e32 v29, v3
	v_mov_b32_e32 v30, v3
	v_mov_b32_e32 v31, v3
	v_mov_b32_e32 v32, v3
	v_mov_b32_e32 v33, v3
	v_mov_b32_e32 v34, v3
	v_mov_b32_e32 v35, v3
	v_mov_b32_e32 v36, v3
	v_mov_b32_e32 v37, v3
	v_mov_b32_e32 v38, v3
	v_mov_b32_e32 v39, v3
	v_mov_b32_e32 v40, v3
	v_mov_b32_e32 v41, v3
	v_mov_b32_e32 v42, v3
	v_mov_b32_e32 v43, v3
	v_mov_b32_e32 v44, v3
	v_mov_b32_e32 v45, v3
	v_mov_b32_e32 v46, v3
	v_mov_b32_e32 v47, v3
	s_waitcnt vmcnt(11)
	ds_write_b128 v108, v[12:15]
	s_waitcnt vmcnt(10)
	ds_write_b128 v108, v[16:19] offset:16384
	s_waitcnt vmcnt(9)
	ds_write_b128 v108, v[20:23] offset:8192
	s_waitcnt vmcnt(8)
	ds_write_b128 v108, v[24:27] offset:24576
	v_mov_b32_e32 v12, v3
	v_mov_b32_e32 v13, v3
	v_mov_b32_e32 v14, v3
	v_mov_b32_e32 v15, v3
	v_mov_b32_e32 v16, v3
	v_mov_b32_e32 v17, v3
	v_mov_b32_e32 v18, v3
	v_mov_b32_e32 v19, v3
	v_mov_b32_e32 v20, v3
	v_mov_b32_e32 v21, v3
	v_mov_b32_e32 v22, v3
	v_mov_b32_e32 v23, v3
	v_mov_b32_e32 v24, v3
	v_mov_b32_e32 v25, v3
	v_mov_b32_e32 v26, v3
	v_mov_b32_e32 v27, v3
	v_mov_b32_e32 v48, v3
	v_mov_b32_e32 v49, v3
	v_mov_b32_e32 v50, v3
	v_mov_b32_e32 v51, v3
	v_mov_b32_e32 v52, v3
	v_mov_b32_e32 v53, v3
	v_mov_b32_e32 v54, v3
	v_mov_b32_e32 v55, v3
	v_mov_b32_e32 v56, v3
	v_mov_b32_e32 v57, v3
	v_mov_b32_e32 v58, v3
	v_mov_b32_e32 v59, v3
	v_mov_b32_e32 v60, v3
	v_mov_b32_e32 v61, v3
	v_mov_b32_e32 v62, v3
	v_mov_b32_e32 v63, v3
	v_mov_b32_e32 v64, v3
	v_mov_b32_e32 v65, v3
	v_and_b32_e32 v112, 63, v0
	s_waitcnt lgkmcnt(0)
	s_barrier
.LBB2_3:
	s_add_i32 s5, s5, 2
	s_add_i32 s0, s5, s11
	s_add_i32 s0, s0, 3
	s_and_b32 s0, s0, 31
	s_lshl_b32 s0, s0, 7
	s_waitcnt vmcnt(4)
	ds_write_b128 v108, v[82:85] offset:40960
	v_lshl_add_u64 v[82:83], v[100:101], 0, s[0:1]
	v_add_co_u32_e32 v114, vcc, s4, v82
	v_lshl_add_u64 v[84:85], v[98:99], 0, s[0:1]
	s_nop 0
	v_addc_co_u32_e32 v115, vcc, 0, v83, vcc
	v_add_co_u32_e32 v116, vcc, s4, v84
	ds_write_b128 v108, v[66:69] offset:32768
	s_nop 0
	v_addc_co_u32_e32 v117, vcc, 0, v85, vcc
	ds_write_b128 v108, v[70:73] offset:49152
	s_waitcnt vmcnt(1)
	ds_write_b128 v108, v[90:93] offset:57344
	global_load_dwordx4 v[66:69], v[82:83], off
	global_load_dwordx4 v[70:73], v[84:85], off
	global_load_dwordx4 v[90:93], v[116:117], off
	ds_read_b128 v[118:121], v109 offset:4096
	global_load_dwordx4 v[82:85], v[114:115], off
	ds_read_b128 v[114:117], v109
	ds_read_b128 v[122:125], v107 offset:16384
	ds_read_b128 v[126:129], v107 offset:20480
	s_waitcnt lgkmcnt(1)
	v_mfma_f32_32x32x16_f16 v[50:65], v[114:117], v[122:125], v[50:65]
	ds_read_b128 v[130:133], v110
	s_waitcnt lgkmcnt(1)
	v_mfma_f32_32x32x16_f16 v[34:49], v[114:117], v[126:129], v[34:49]
	ds_read_b128 v[114:117], v110 offset:4096
	v_mfma_f32_32x32x16_f16 v[18:33], v[118:121], v[122:125], v[18:33]
	ds_read_b128 v[122:125], v111 offset:16384
	v_mfma_f32_32x32x16_f16 v[2:17], v[118:121], v[126:129], v[2:17]
	ds_read_b128 v[118:121], v111 offset:20480
	s_add_i32 s0, s5, s11
	s_add_i32 s0, s0, 4
	s_and_b32 s0, s0, 31
	s_lshl_b32 s0, s0, 7
	s_waitcnt lgkmcnt(0)
	s_barrier
	ds_write_b128 v108, v[86:89] offset:8192
	v_lshl_add_u64 v[86:87], v[100:101], 0, s[0:1]
	v_mfma_f32_32x32x16_f16 v[50:65], v[130:133], v[122:125], v[50:65]
	v_lshl_add_u64 v[88:89], v[98:99], 0, s[0:1]
	ds_write_b128 v108, v[74:77]
	ds_write_b128 v108, v[78:81] offset:16384
	s_waitcnt vmcnt(4)
	ds_write_b128 v108, v[94:97] offset:24576
	global_load_dwordx4 v[74:77], v[86:87], off
	global_load_dwordx4 v[78:81], v[88:89], off
	ds_read_b128 v[126:129], v109 offset:36864
	v_mfma_f32_32x32x16_f16 v[18:33], v[114:117], v[122:125], v[18:33]
	v_add_co_u32_e32 v122, vcc, s4, v86
	s_nop 1
	v_addc_co_u32_e32 v123, vcc, 0, v87, vcc
	v_add_co_u32_e32 v124, vcc, s4, v88
	v_mfma_f32_32x32x16_f16 v[34:49], v[130:133], v[118:121], v[34:49]
	s_nop 0
	v_addc_co_u32_e32 v125, vcc, 0, v89, vcc
	global_load_dwordx4 v[86:89], v[122:123], off
	global_load_dwordx4 v[94:97], v[124:125], off
	ds_read_b128 v[122:125], v109 offset:32768
	v_mfma_f32_32x32x16_f16 v[2:17], v[114:117], v[118:121], v[2:17]
	ds_read_b128 v[114:117], v107 offset:49152
	ds_read_b128 v[118:121], v107 offset:53248
	s_waitcnt lgkmcnt(1)
	v_mfma_f32_32x32x16_f16 v[50:65], v[122:125], v[114:117], v[50:65]
	ds_read_b128 v[130:133], v110 offset:32768
	s_waitcnt lgkmcnt(1)
	v_mfma_f32_32x32x16_f16 v[34:49], v[122:125], v[118:121], v[34:49]
	ds_read_b128 v[122:125], v110 offset:36864
	v_mfma_f32_32x32x16_f16 v[18:33], v[126:129], v[114:117], v[18:33]
	ds_read_b128 v[114:117], v111 offset:49152
	v_mfma_f32_32x32x16_f16 v[2:17], v[126:129], v[118:121], v[2:17]
	ds_read_b128 v[118:121], v111 offset:53248
	s_waitcnt lgkmcnt(1)
	v_mfma_f32_32x32x16_f16 v[50:65], v[130:133], v[114:117], v[50:65]
	s_cmp_gt_u32 s5, 29
	s_waitcnt lgkmcnt(0)
	s_barrier
	v_mfma_f32_32x32x16_f16 v[34:49], v[130:133], v[118:121], v[34:49]
	v_mfma_f32_32x32x16_f16 v[18:33], v[122:125], v[114:117], v[18:33]
	v_mfma_f32_32x32x16_f16 v[2:17], v[122:125], v[118:121], v[2:17]
	s_cbranch_scc0 .LBB2_3
	v_cmp_ne_u32_e32 vcc, 0, v105
	s_waitcnt vmcnt(7)
	v_lshlrev_b32_e32 v66, 2, v112
	v_lshlrev_b32_e32 v67, 14, v104
	s_and_saveexec_b64 s[0:1], vcc
	s_cbranch_execz .LBB2_6
	v_and_b32_e32 v68, 0xc000, v67
	v_add3_u32 v68, 0, v66, v68
	ds_write2st64_b32 v68, v50, v51 offset1:1
	ds_write2st64_b32 v68, v52, v53 offset0:2 offset1:3
	ds_write2st64_b32 v68, v54, v55 offset0:4 offset1:5
	ds_write2st64_b32 v68, v56, v57 offset0:6 offset1:7
	ds_write2st64_b32 v68, v58, v59 offset0:8 offset1:9
	ds_write2st64_b32 v68, v60, v61 offset0:10 offset1:11
	ds_write2st64_b32 v68, v62, v63 offset0:12 offset1:13
	ds_write2st64_b32 v68, v64, v65 offset0:14 offset1:15
	ds_write2st64_b32 v68, v34, v35 offset0:16 offset1:17
	ds_write2st64_b32 v68, v36, v37 offset0:18 offset1:19
	ds_write2st64_b32 v68, v38, v39 offset0:20 offset1:21
	ds_write2st64_b32 v68, v40, v41 offset0:22 offset1:23
	ds_write2st64_b32 v68, v42, v43 offset0:24 offset1:25
	ds_write2st64_b32 v68, v44, v45 offset0:26 offset1:27
	ds_write2st64_b32 v68, v46, v47 offset0:28 offset1:29
	ds_write2st64_b32 v68, v48, v49 offset0:30 offset1:31
	ds_write2st64_b32 v68, v18, v19 offset0:32 offset1:33
	ds_write2st64_b32 v68, v20, v21 offset0:34 offset1:35
	ds_write2st64_b32 v68, v22, v23 offset0:36 offset1:37
	ds_write2st64_b32 v68, v24, v25 offset0:38 offset1:39
	ds_write2st64_b32 v68, v26, v27 offset0:40 offset1:41
	ds_write2st64_b32 v68, v28, v29 offset0:42 offset1:43
	ds_write2st64_b32 v68, v30, v31 offset0:44 offset1:45
	ds_write2st64_b32 v68, v32, v33 offset0:46 offset1:47
	ds_write2st64_b32 v68, v2, v3 offset0:48 offset1:49
	ds_write2st64_b32 v68, v4, v5 offset0:50 offset1:51
	ds_write2st64_b32 v68, v6, v7 offset0:52 offset1:53
	ds_write2st64_b32 v68, v8, v9 offset0:54 offset1:55
	ds_write2st64_b32 v68, v10, v11 offset0:56 offset1:57
	ds_write2st64_b32 v68, v12, v13 offset0:58 offset1:59
	ds_write2st64_b32 v68, v14, v15 offset0:60 offset1:61
	ds_write2st64_b32 v68, v16, v17 offset0:62 offset1:63

	.amdhsa_kernel _Z9wo_kernelPKDF16_S0_Pf
		.amdhsa_group_segment_fixed_size 0
		.amdhsa_private_segment_fixed_size 0
		.amdhsa_kernarg_size 24
		.amdhsa_user_sgpr_count 2
		.amdhsa_user_sgpr_dispatch_ptr 0
		.amdhsa_user_sgpr_queue_ptr 0
		.amdhsa_user_sgpr_kernarg_segment_ptr 1
		.amdhsa_user_sgpr_dispatch_id 0
		.amdhsa_user_sgpr_kernarg_preload_length 0
		.amdhsa_user_sgpr_kernarg_preload_offset 0
		.amdhsa_user_sgpr_private_segment_size 0
		.amdhsa_uses_dynamic_stack 0
		.amdhsa_enable_private_segment 0
		.amdhsa_system_sgpr_workgroup_id_x 1
		.amdhsa_system_sgpr_workgroup_id_y 0
		.amdhsa_system_sgpr_workgroup_id_z 0
		.amdhsa_system_sgpr_workgroup_info 0
		.amdhsa_system_vgpr_workitem_id 0
		.amdhsa_next_free_vgpr 136
		.amdhsa_next_free_sgpr 18
		.amdhsa_accum_offset 136
		.amdhsa_reserve_vcc 1
		.amdhsa_float_round_mode_32 0
		.amdhsa_float_round_mode_16_64 0
		.amdhsa_float_denorm_mode_32 3
		.amdhsa_float_denorm_mode_16_64 3
		.amdhsa_dx10_clamp 1
		.amdhsa_ieee_mode 1
		.amdhsa_fp16_overflow 0
		.amdhsa_tg_split 0
		.amdhsa_exception_fp_ieee_invalid_op 0
		.amdhsa_exception_fp_denorm_src 0
		.amdhsa_exception_fp_ieee_div_zero 0
		.amdhsa_exception_fp_ieee_overflow 0
		.amdhsa_exception_fp_ieee_underflow 0
		.amdhsa_exception_fp_ieee_inexact 0
		.amdhsa_exception_int_div_zero 0
	.end_amdhsa_kernel
